# LDS-DMA staging: all 16 Wv fragments + 2 Wfc fragments per wave (the latter in the wave's own Ch row and padding-row slots)
# baseline (speedup 1.0000x reference)
.Lring_go_0:
	v_mul_f32_e32 v74, v10, v70
	v_mul_f32_e32 v75, v6, v70
	v_mul_f32_e32 v76, v10, v66
	v_mul_f32_e32 v77, v6, v66
	v_mul_f32_e32 v78, v10, v62
	v_mul_f32_e32 v79, v6, v62
	v_mul_f32_e32 v80, v10, v58
	v_mul_f32_e32 v81, v6, v58
	v_mul_f32_e32 v82, v10, v54
	v_mul_f32_e32 v83, v6, v54
	v_mul_f32_e32 v84, v10, v46
	v_mul_f32_e32 v85, v6, v46
	v_mul_f32_e32 v86, v10, v34
	v_mul_f32_e32 v87, v6, v34
	v_mul_f32_e32 v88, v10, v14
	v_mul_f32_e32 v89, v6, v14
	v_fmac_f32_e32 v74, v71, v11
	v_fmac_f32_e32 v75, v71, v7
	v_fmac_f32_e32 v76, v67, v11
	v_fmac_f32_e32 v77, v67, v7
	v_fmac_f32_e32 v78, v63, v11
	v_fmac_f32_e32 v79, v63, v7
	v_fmac_f32_e32 v80, v59, v11
	v_fmac_f32_e32 v81, v59, v7
	v_fmac_f32_e32 v82, v55, v11
	v_fmac_f32_e32 v83, v55, v7
	v_fmac_f32_e32 v84, v47, v11
	v_fmac_f32_e32 v85, v47, v7
	v_fmac_f32_e32 v86, v35, v11
	v_fmac_f32_e32 v87, v35, v7
	v_fmac_f32_e32 v88, v15, v11
	v_fmac_f32_e32 v89, v15, v7
	v_fmac_f32_e32 v74, v72, v12
	v_fmac_f32_e32 v75, v72, v8
	v_fmac_f32_e32 v76, v68, v12
	v_fmac_f32_e32 v77, v68, v8
	v_fmac_f32_e32 v78, v64, v12
	v_fmac_f32_e32 v79, v64, v8
	v_fmac_f32_e32 v80, v60, v12
	v_fmac_f32_e32 v81, v60, v8
	v_fmac_f32_e32 v82, v56, v12
	v_fmac_f32_e32 v83, v56, v8
	v_fmac_f32_e32 v84, v48, v12
	v_fmac_f32_e32 v85, v48, v8
	v_fmac_f32_e32 v86, v36, v12
	v_fmac_f32_e32 v87, v36, v8
	v_fmac_f32_e32 v88, v16, v12
	v_fmac_f32_e32 v89, v16, v8
	v_fmac_f32_e32 v74, v73, v13
	v_fmac_f32_e32 v75, v73, v9
	v_fmac_f32_e32 v76, v69, v13
	v_fmac_f32_e32 v77, v69, v9
	v_fmac_f32_e32 v78, v65, v13
	v_fmac_f32_e32 v79, v65, v9
	v_fmac_f32_e32 v80, v61, v13
	v_fmac_f32_e32 v81, v61, v9
	v_fmac_f32_e32 v82, v57, v13
	v_fmac_f32_e32 v83, v57, v9
	v_fmac_f32_e32 v84, v49, v13
	v_fmac_f32_e32 v85, v49, v9
	v_fmac_f32_e32 v86, v37, v13
	v_fmac_f32_e32 v87, v37, v9
	v_fmac_f32_e32 v88, v17, v13
	v_fmac_f32_e32 v89, v17, v9
	v_permlane32_swap_b32_e32 v74, v82
	v_permlane32_swap_b32_e32 v75, v83
	v_permlane32_swap_b32_e32 v76, v84
	v_permlane32_swap_b32_e32 v77, v85
	v_permlane32_swap_b32_e32 v78, v86
	v_permlane32_swap_b32_e32 v79, v87
	v_permlane32_swap_b32_e32 v80, v88
	v_permlane32_swap_b32_e32 v81, v89
	v_add_f32_e32 v74, v74, v82
	v_add_f32_e32 v75, v75, v83
	v_add_f32_e32 v76, v76, v84
	v_add_f32_e32 v77, v77, v85
	v_add_f32_e32 v78, v78, v86
	v_add_f32_e32 v79, v79, v87
	v_add_f32_e32 v80, v80, v88
	v_add_f32_e32 v81, v81, v89
	v_permlane16_swap_b32_e32 v74, v78
	v_permlane16_swap_b32_e32 v75, v79
	v_permlane16_swap_b32_e32 v76, v80
	v_permlane16_swap_b32_e32 v77, v81
	v_add_f32_e32 v74, v74, v78
	v_add_f32_e32 v75, v75, v79
	v_add_f32_e32 v76, v76, v80
	v_add_f32_e32 v77, v77, v81
	v_add_f32_dpp v74, v74, v74 row_ror:8 row_mask:0xf bank_mask:0xf bound_ctrl:1
	v_add_f32_dpp v76, v76, v76 row_ror:8 row_mask:0xf bank_mask:0xf bound_ctrl:1
	v_add_f32_dpp v75, v75, v75 row_ror:8 row_mask:0xf bank_mask:0xf bound_ctrl:1
	v_add_f32_dpp v77, v77, v77 row_ror:8 row_mask:0xf bank_mask:0xf bound_ctrl:1
	v_cndmask_b32_e64 v74, v76, v74, s[4:5]
	v_cndmask_b32_e64 v75, v77, v75, s[4:5]
	v_cmp_eq_u32_e64 s[0:1], 0, v107
	v_add_f32_dpp v74, v74, v74 row_half_mirror row_mask:0xf bank_mask:0xf bound_ctrl:1
	v_add_f32_dpp v75, v75, v75 row_half_mirror row_mask:0xf bank_mask:0xf bound_ctrl:1
	v_cndmask_b32_e64 v74, v75, v74, s[2:3]
	s_nop 1
	v_add_f32_dpp v74, v74, v74 quad_perm:[2,3,0,1] row_mask:0xf bank_mask:0xf bound_ctrl:1
	s_nop 1
	v_add_f32_dpp v74, v74, v74 quad_perm:[1,0,3,2] row_mask:0xf bank_mask:0xf bound_ctrl:1
	v_cndmask_b32_e64 v74, v113, v74, s[0:1]
	s_and_saveexec_b64 s[0:1], vcc
	ds_write_b32 v114, v74
	s_or_b64 exec, exec, s[0:1]
	v_mov_b32_dpp v90, v74 row_ror:8 row_mask:0xf bank_mask:0xf bound_ctrl:1
	v_add_u32_e32 v114, 32, v114
	v_max_f32_e32 v90, v74, v90
	v_mov_b32_e32 v91, v90
	s_nop 1
	v_permlane16_swap_b32_e32 v90, v91
	s_nop 0
	v_max_f32_e32 v90, v90, v91
	v_mov_b32_e32 v91, v90
	s_nop 1
	v_permlane32_swap_b32_e32 v90, v91
	s_nop 0
	v_max3_f32 v92, v104, v90, v91
	v_sub_f32_e32 v93, v104, v92
	v_sub_f32_e32 v94, v74, v92
	v_exp_f32_e32 v93, v93
	v_exp_f32_e32 v94, v94
	v_mov_b32_e32 v104, v92
	s_nop 1
	v_fma_f32 v105, v105, v93, v94
	s_nop 0
	v_readlane_b32 s34, v93, 0
	v_readlane_b32 s36, v93, 4
	v_readlane_b32 s38, v94, 0
	v_readlane_b32 s40, v94, 4
	v_readlane_b32 s42, v94, 8
	v_readlane_b32 s44, v94, 12
	v_readlane_b32 s46, v94, 16
	v_readlane_b32 s48, v94, 20
	v_readlane_b32 s50, v94, 24
	v_readlane_b32 s52, v94, 28
	v_readlane_b32 s54, v94, 32
	v_readlane_b32 s56, v94, 36
	v_readlane_b32 s58, v94, 40
	v_readlane_b32 s60, v94, 44
	v_readlane_b32 s62, v94, 48
	v_readlane_b32 s64, v94, 52
	v_readlane_b32 s66, v94, 56
	v_readlane_b32 s68, v94, 60
	s_nop 1
	v_pk_mul_f32 v[96:97], v[96:97], s[34:35] op_sel_hi:[1,0]
	v_pk_mul_f32 v[98:99], v[98:99], s[34:35] op_sel_hi:[1,0]
	v_pk_mul_f32 v[100:101], v[100:101], s[36:37] op_sel_hi:[1,0]
	v_pk_mul_f32 v[102:103], v[102:103], s[36:37] op_sel_hi:[1,0]
	v_pk_fma_f32 v[96:97], v[70:71], s[38:39], v[96:97] op_sel_hi:[1,0,1]
	v_pk_fma_f32 v[98:99], v[72:73], s[38:39], v[98:99] op_sel_hi:[1,0,1]
	v_pk_fma_f32 v[100:101], v[70:71], s[40:41], v[100:101] op_sel_hi:[1,0,1]
	v_pk_fma_f32 v[102:103], v[72:73], s[40:41], v[102:103] op_sel_hi:[1,0,1]
	v_pk_fma_f32 v[96:97], v[66:67], s[42:43], v[96:97] op_sel_hi:[1,0,1]
	v_pk_fma_f32 v[98:99], v[68:69], s[42:43], v[98:99] op_sel_hi:[1,0,1]
	v_pk_fma_f32 v[100:101], v[66:67], s[44:45], v[100:101] op_sel_hi:[1,0,1]
	v_pk_fma_f32 v[102:103], v[68:69], s[44:45], v[102:103] op_sel_hi:[1,0,1]
	v_pk_fma_f32 v[96:97], v[62:63], s[46:47], v[96:97] op_sel_hi:[1,0,1]
	v_pk_fma_f32 v[98:99], v[64:65], s[46:47], v[98:99] op_sel_hi:[1,0,1]
	v_pk_fma_f32 v[100:101], v[62:63], s[48:49], v[100:101] op_sel_hi:[1,0,1]
	v_pk_fma_f32 v[102:103], v[64:65], s[48:49], v[102:103] op_sel_hi:[1,0,1]
	v_pk_fma_f32 v[96:97], v[58:59], s[50:51], v[96:97] op_sel_hi:[1,0,1]
	v_pk_fma_f32 v[98:99], v[60:61], s[50:51], v[98:99] op_sel_hi:[1,0,1]
	v_pk_fma_f32 v[100:101], v[58:59], s[52:53], v[100:101] op_sel_hi:[1,0,1]
	v_pk_fma_f32 v[102:103], v[60:61], s[52:53], v[102:103] op_sel_hi:[1,0,1]
	v_pk_fma_f32 v[96:97], v[54:55], s[54:55], v[96:97] op_sel_hi:[1,0,1]
	v_pk_fma_f32 v[98:99], v[56:57], s[54:55], v[98:99] op_sel_hi:[1,0,1]
	v_pk_fma_f32 v[100:101], v[54:55], s[56:57], v[100:101] op_sel_hi:[1,0,1]
	v_pk_fma_f32 v[102:103], v[56:57], s[56:57], v[102:103] op_sel_hi:[1,0,1]
	v_pk_fma_f32 v[96:97], v[46:47], s[58:59], v[96:97] op_sel_hi:[1,0,1]
	v_pk_fma_f32 v[98:99], v[48:49], s[58:59], v[98:99] op_sel_hi:[1,0,1]
	v_pk_fma_f32 v[100:101], v[46:47], s[60:61], v[100:101] op_sel_hi:[1,0,1]
	v_pk_fma_f32 v[102:103], v[48:49], s[60:61], v[102:103] op_sel_hi:[1,0,1]
	v_pk_fma_f32 v[96:97], v[34:35], s[62:63], v[96:97] op_sel_hi:[1,0,1]
	v_pk_fma_f32 v[98:99], v[36:37], s[62:63], v[98:99] op_sel_hi:[1,0,1]
	v_pk_fma_f32 v[100:101], v[34:35], s[64:65], v[100:101] op_sel_hi:[1,0,1]
	v_pk_fma_f32 v[102:103], v[36:37], s[64:65], v[102:103] op_sel_hi:[1,0,1]
	v_pk_fma_f32 v[96:97], v[14:15], s[66:67], v[96:97] op_sel_hi:[1,0,1]
	v_pk_fma_f32 v[98:99], v[16:17], s[66:67], v[98:99] op_sel_hi:[1,0,1]
	v_pk_fma_f32 v[100:101], v[14:15], s[68:69], v[100:101] op_sel_hi:[1,0,1]
	v_pk_fma_f32 v[102:103], v[16:17], s[68:69], v[102:103] op_sel_hi:[1,0,1]
	s_cmp_lg_u32 s30, 8
	s_cbranch_scc1 .Lring_nostage
	v_lshlrev_b32_e32 v176, 4, v196
	v_lshl_add_u32 v176, v197, 14, v176
	s_mov_b32 m0, s33
	s_nop 0
	global_load_lds_dwordx4 v176, s[8:9]
	global_load_lds_dwordx4 v176, s[8:9] offset:1024
	global_load_lds_dwordx4 v176, s[8:9] offset:2048
	global_load_lds_dwordx4 v176, s[8:9] offset:3072
	v_add_u32_e32 v176, 0x1000, v176
	s_add_u32 s35, s33, 4096
	s_mov_b32 m0, s35
	s_nop 0
	global_load_lds_dwordx4 v176, s[8:9]
	global_load_lds_dwordx4 v176, s[8:9] offset:1024
	global_load_lds_dwordx4 v176, s[8:9] offset:2048
	global_load_lds_dwordx4 v176, s[8:9] offset:3072
	v_add_u32_e32 v176, 0x1000, v176
	s_add_u32 s35, s33, 8192
	s_mov_b32 m0, s35
	s_nop 0
	global_load_lds_dwordx4 v176, s[8:9]
	global_load_lds_dwordx4 v176, s[8:9] offset:1024
	global_load_lds_dwordx4 v176, s[8:9] offset:2048
	v_add_u32_e32 v176, 0xc00, v176
	s_mul_i32 s35, s32, 3072
	s_add_u32 s35, s35, 46080
	s_mov_b32 m0, s35
	s_nop 0
	global_load_lds_dwordx4 v176, s[8:9]
	global_load_lds_dwordx4 v176, s[8:9] offset:1024
	global_load_lds_dwordx4 v176, s[8:9] offset:2048
	v_add_u32_e32 v176, 0xc00, v176
	s_mul_i32 s35, s32, 2048
	s_add_u32 s35, s35, 16640
	s_mov_b32 m0, s35
	s_nop 0
	global_load_lds_dwordx4 v176, s[8:9]
	global_load_lds_dwordx4 v176, s[8:9] offset:1024
	v_lshlrev_b32_e32 v176, 4, v196
	v_lshl_add_u32 v176, v197, 14, v176
	v_add_u32_e32 v176, 0x20000, v176
	s_mul_i32 s35, s32, 1040
	s_mov_b32 m0, s35
	s_nop 0
	global_load_lds_dwordx4 v176, s[8:9]
	s_add_u32 s35, s35, 7296
	s_mov_b32 m0, s35
	s_nop 0
	global_load_lds_dwordx4 v176, s[8:9] offset:1024

.Lring_done:
	s_setprio 0
	v_mov_b32_e32 v240, v96
	v_mov_b32_e32 v241, v97
	v_mov_b32_e32 v242, v98
	v_mov_b32_e32 v243, v99
	v_mov_b32_e32 v244, v100
	v_mov_b32_e32 v245, v101
	v_mov_b32_e32 v246, v102
	v_mov_b32_e32 v247, v103
	v_mov_b32_e32 v248, v104
	v_mov_b32_e32 v249, v105
	s_movk_i32 s0, 0x640
	v_mov_b32_e32 v14, 0x8200
	v_mad_u32_u24 v205, v197, s0, v14
	v_lshlrev_b32_e32 v10, 4, v106
	v_or_b32_e32 v6, 0x2000, v196
	v_add_lshl_u32 v7, v122, v6, 4
	v_lshlrev_b32_e32 v11, 4, v196
	v_add_u32_e32 v11, s33, v11
	s_mul_i32 s35, s32, 3072
	s_add_u32 s35, s35, 46080
	v_lshlrev_b32_e32 v12, 4, v196
	v_add_u32_e32 v12, s35, v12
	s_mul_i32 s35, s32, 2048
	s_add_u32 s35, s35, 16640
	v_lshlrev_b32_e32 v13, 4, v196
	s_nop 0
	v_add_u32_e32 v13, s35, v13
	ds_read_b128 v[158:161], v11
	ds_read_b128 v[154:157], v11 offset:1024
	ds_read_b128 v[146:149], v11 offset:2048
	ds_read_b128 v[138:141], v11 offset:3072
	ds_read_b128 v[118:121], v11 offset:4096
	ds_read_b128 v[106:109], v11 offset:5120
	ds_read_b128 v[98:101], v11 offset:6144
	ds_read_b128 v[102:105], v11 offset:7168
	ds_read_b128 v[170:173], v11 offset:8192
	ds_read_b128 v[166:169], v11 offset:9216
	ds_read_b128 v[178:181], v11 offset:10240
	ds_read_b128 v[174:177], v12
	ds_read_b128 v[162:165], v12 offset:1024
	s_nop 0
	ds_read_b128 v[134:137], v12 offset:2048
	ds_read_b128 v[114:117], v13
	ds_read_b128 v[110:113], v13 offset:1024
	s_mul_i32 s35, s32, 1040
	v_lshlrev_b32_e32 v10, 4, v196
	s_nop 0
	v_add_u32_e32 v10, s35, v10
	ds_read_b128 v[94:97], v10
	ds_read_b128 v[90:93], v10 offset:8320
	global_load_dwordx4 v[78:81], v7, s[8:9] offset:2048
	global_load_dwordx4 v[74:77], v7, s[8:9] offset:3072
	v_add_lshl_u32 v7, v123, v6, 4
	v_add_lshl_u32 v8, v124, v6, 4
	global_load_dwordx4 v[66:69], v7, s[8:9]
	global_load_dwordx4 v[58:61], v8, s[8:9]
	v_add_lshl_u32 v7, v125, v6, 4
	v_add_lshl_u32 v8, v126, v6, 4
	global_load_dwordx4 v[62:65], v7, s[8:9]
	global_load_dwordx4 v[54:57], v8, s[8:9]
	v_add_lshl_u32 v7, v127, v6, 4
	v_add_lshl_u32 v8, v128, v6, 4
	global_load_dwordx4 v[150:153], v7, s[8:9]
	global_load_dwordx4 v[142:145], v8, s[8:9]
	v_add_lshl_u32 v7, v129, v6, 4
	v_add_lshl_u32 v8, v130, v6, 4
	global_load_dwordx4 v[130:133], v7, s[8:9]
	global_load_dwordx4 v[126:129], v8, s[8:9]
	v_add_lshl_u32 v7, v192, v6, 4
	v_add_lshl_u32 v8, v202, v6, 4
	global_load_dwordx4 v[122:125], v7, s[8:9]
	global_load_dwordx4 v[82:85], v8, s[8:9]
	v_add_lshl_u32 v7, v203, v6, 4
	v_add_lshl_u32 v6, v204, v6, 4
	global_load_dwordx4 v[86:89], v7, s[8:9]
	global_load_dwordx4 v[70:73], v6, s[8:9]
	v_lshlrev_b32_e32 v187, 2, v195
	v_and_or_b32 v190, v187, 4, s31
	v_or_b32_e32 v208, 1, v190
	v_mul_u32_u24_e32 v6, 0x300, v197
	v_ashrrev_i32_e32 v191, 31, v190
	v_ashrrev_i32_e32 v209, 31, v208
	v_or_b32_e32 v6, v196, v6
	v_lshlrev_b64 v[210:211], 9, v[190:191]
	v_lshlrev_b32_e32 v191, 2, v1
	v_lshlrev_b64 v[222:223], 9, v[208:209]
	v_or_b32_e32 v208, 2, v190
	v_mov_b32_e32 v193, 0
	v_lshlrev_b32_e32 v14, 4, v6
	v_lshl_or_b32 v192, v197, 7, v191
	s_movk_i32 s2, 0xfe00
	v_ashrrev_i32_e32 v209, 31, v208
	v_or_b32_e32 v6, 0x40000, v14
	s_movk_i32 s1, 0x100
	v_lshl_add_u64 v[220:221], s[22:23], 0, v[192:193]
	s_mov_b32 s3, -1
	v_lshlrev_b64 v[226:227], 9, v[208:209]
	v_or_b32_e32 v208, 3, v190
	global_load_dwordx4 v[50:53], v6, s[8:9]
	global_load_dwordx4 v[46:49], v6, s[8:9] offset:1024
	global_load_dwordx4 v[42:45], v6, s[8:9] offset:2048
	global_load_dwordx4 v[30:33], v6, s[8:9] offset:3072
	v_add_u32_e32 v6, 0x41000, v14
	v_add_u32_e32 v7, 0x41400, v14
	v_lshl_add_u64 v[212:213], s[20:21], 0, v[192:193]
	v_lshl_add_u64 v[202:203], v[220:221], 0, s[2:3]
	v_cmp_gt_u32_e32 vcc, s1, v0
	v_ashrrev_i32_e32 v209, 31, v208
	s_movk_i32 s2, 0xfe40
	global_load_dwordx4 v[38:41], v6, s[8:9]
	global_load_dwordx4 v[22:25], v7, s[8:9]
	v_add_u32_e32 v6, 0x41800, v14
	v_add_u32_e32 v7, 0x41c00, v14
	v_cndmask_b32_e32 v203, v203, v213, vcc
	v_cndmask_b32_e32 v202, v202, v212, vcc
	v_lshlrev_b64 v[230:231], 9, v[208:209]
	s_mov_b32 s3, -1
	global_load_dwordx4 v[34:37], v6, s[8:9]
	global_load_dwordx4 v[10:13], v7, s[8:9]
	v_add_u32_e32 v6, 0x42000, v14
	v_add_u32_e32 v7, 0x42400, v14
	v_add_u32_e32 v15, 0x42800, v14
	v_add_u32_e32 v18, 0x42c00, v14
	v_lshl_add_u64 v[206:207], v[202:203], 0, v[210:211]
	v_lshl_add_u64 v[224:225], v[202:203], 0, v[222:223]
	v_lshl_add_u64 v[228:229], v[202:203], 0, v[226:227]
	v_lshl_add_u64 v[202:203], v[202:203], 0, v[230:231]
	v_lshl_add_u64 v[212:213], v[212:213], 0, 64
	v_lshl_add_u64 v[220:221], v[220:221], 0, s[2:3]
	global_load_dwordx4 v[26:29], v6, s[8:9]
	s_nop 0
	global_load_dwordx4 v[6:9], v7, s[8:9]
	s_nop 0
	global_load_dwordx4 v[14:17], v15, s[8:9]
	s_nop 0
	global_load_dwordx4 v[18:21], v18, s[8:9]
	s_nop 0
	global_load_dword v208, v[206:207], off
	s_nop 0
	global_load_dword v207, v[224:225], off
	global_load_dword v204, v[228:229], off
	s_nop 0
	global_load_dword v203, v[202:203], off
	s_nop 0
	global_load_dword v206, v192, s[10:11]
	global_load_dword v202, v192, s[10:11] offset:64
	v_cndmask_b32_e32 v213, v221, v213, vcc
	v_cndmask_b32_e32 v212, v220, v212, vcc
	v_lshl_add_u64 v[210:211], v[212:213], 0, v[210:211]
	v_lshl_add_u64 v[220:221], v[212:213], 0, v[222:223]
	v_lshl_add_u64 v[222:223], v[212:213], 0, v[226:227]
	v_lshl_add_u64 v[224:225], v[212:213], 0, v[230:231]
	global_load_dword v212, v[210:211], off
	s_nop 0
	global_load_dword v211, v[220:221], off
	global_load_dword v210, v[222:223], off
	global_load_dword v209, v[224:225], off
	v_lshl_or_b32 v190, v197, 4, v1
	v_lshlrev_b32_e32 v186, 2, v190
	global_load_dword v189, v186, s[24:25]
	global_load_dword v188, v186, s[26:27]
	v_mov_b32_e32 v233, v249
	v_mov_b32_e32 v232, v248
	v_mov_b32_e32 v214, v240
	v_mov_b32_e32 v215, v241
	v_mov_b32_e32 v216, v242
	v_mov_b32_e32 v217, v243
	v_mov_b32_e32 v218, v244
	v_mov_b32_e32 v219, v245
	v_mov_b32_e32 v220, v246
	v_mov_b32_e32 v221, v247
	s_nop 1
	v_add_f32_dpp v2, v233, v233 row_ror:8 row_mask:0xf bank_mask:0xf bound_ctrl:1
	v_mov_b32_e32 v3, v2
	s_nop 1
	v_permlane16_swap_b32_e32 v2, v3
	v_add_f32_e32 v2, v2, v3
	v_mov_b32_e32 v3, v2
	s_nop 1
	v_permlane32_swap_b32_e32 v2, v3
	v_add_f32_e32 v2, v2, v3
	v_readlane_b32 s2, v232, 4
	v_readlane_b32 s4, v2, 4
	v_readlane_b32 s5, v2, 0
	v_readlane_b32 s3, v232, 0
	v_div_scale_f32 v3, s[0:1], s4, s4, 1.0
	v_rcp_f32_e32 v4, v3
	v_lshl_add_u64 v[182:183], v[182:183], 2, s[28:29]
	v_fma_f32 v2, -v3, v4, 1.0
	v_fmac_f32_e32 v4, v2, v4
	v_div_scale_f32 v2, vcc, 1.0, s4, 1.0
	v_mul_f32_e32 v5, v2, v4
	v_fma_f32 v192, -v3, v5, v2
	v_fmac_f32_e32 v5, v192, v4
	v_fma_f32 v2, -v3, v5, v2
	v_div_scale_f32 v3, s[0:1], s5, s5, 1.0
	v_rcp_f32_e32 v192, v3
	v_div_fmas_f32 v2, v2, v4, v5
	v_div_fixup_f32 v2, v2, s4, 1.0
	s_movk_i32 s0, 0xc8
	v_fma_f32 v4, -v3, v192, 1.0
	v_fmac_f32_e32 v192, v4, v192
	v_div_scale_f32 v4, vcc, 1.0, s5, 1.0
	v_mul_f32_e32 v5, v4, v192
	v_fma_f32 v213, -v3, v5, v4
	v_fmac_f32_e32 v5, v213, v192
	v_fma_f32 v3, -v3, v5, v4
	v_div_fmas_f32 v3, v3, v192, v5
	v_div_fixup_f32 v4, v3, s5, 1.0
	v_pk_mul_f32 v[216:217], v[216:217], v[4:5] op_sel_hi:[1,0]
	v_pk_mul_f32 v[214:215], v[214:215], v[4:5] op_sel_hi:[1,0]
	v_cvt_pk_f16_f32 v217, v216, v217
	v_cvt_pk_f16_f32 v216, v214, v215
	v_pk_mul_f32 v[214:215], v[220:221], v[2:3] op_sel_hi:[1,0]
	v_pk_mul_f32 v[218:219], v[218:219], v[2:3] op_sel_hi:[1,0]
	v_add_u32_e32 v3, v205, v184
	ds_read2_b32 v[220:221], v3 offset0:128 offset1:200
	v_cvt_pk_f16_f32 v215, v214, v215
	v_cvt_pk_f16_f32 v214, v218, v219
	ds_read2st64_b32 v[218:219], v3 offset1:1
	v_add_u32_e32 v192, 32, v3
	ds_write2st64_b64 v185, v[216:217], v[214:215] offset1:1
	ds_read2st64_b32 v[214:215], v192 offset0:4 offset1:5
	s_waitcnt lgkmcnt(3)
	v_subrev_f32_e32 v5, s2, v221
	v_exp_f32_e32 v5, v5
	s_waitcnt lgkmcnt(2)
	v_subrev_f32_e32 v185, s3, v218
	v_exp_f32_e32 v185, v185
	s_waitcnt lgkmcnt(0)
	v_subrev_f32_e32 v205, s2, v214
	v_mul_f32_e32 v5, v2, v5
	v_subrev_f32_e32 v192, s3, v219
	v_exp_f32_e32 v205, v205
	v_fmac_f32_e32 v5, v4, v185
	v_mov_b32_e32 v185, v193
	v_exp_f32_e32 v192, v192
	v_lshl_add_u64 v[182:183], v[182:183], 0, v[184:185]
	v_subrev_f32_e32 v185, s2, v215
	v_mul_f32_e32 v5, 0.5, v5
	v_subrev_f32_e32 v184, s3, v220
	v_exp_f32_e32 v185, v185
	global_store_dword v[182:183], v5, off
	v_mul_f32_e32 v5, v2, v205
	v_exp_f32_e32 v184, v184
	v_fmac_f32_e32 v5, v4, v192
	v_mul_f32_e32 v5, 0.5, v5
	global_store_dword v[182:183], v5, off offset:256
	v_mul_f32_e32 v5, v2, v185
	v_fmac_f32_e32 v5, v4, v184
	v_mul_f32_e32 v5, 0.5, v5
	global_store_dword v[182:183], v5, off offset:512
	v_or_b32_e32 v5, 0xc0, v196
	v_cmp_gt_u32_e32 vcc, s0, v5
	s_and_saveexec_b64 s[0:1], vcc
	s_cbranch_execz .LBB1_19
	v_add_u32_e32 v3, 0x300, v3
	ds_read2_b32 v[184:185], v3 offset1:200
	s_waitcnt lgkmcnt(0)
	v_subrev_f32_e32 v3, s3, v184
	v_subrev_f32_e32 v5, s2, v185
	v_exp_f32_e32 v184, v3
	v_exp_f32_e32 v185, v5
	v_mov_b32_e32 v5, v2
	v_pk_mul_f32 v[2:3], v[4:5], v[184:185]
	s_nop 0
	v_add_f32_e32 v2, v2, v3
	v_mul_f32_e32 v2, 0.5, v2
	global_store_dword v[182:183], v2, off offset:768
